# gemm loop-edge edit: the six 64-bit address bumps moved from the loop back edge into MFMA gaps of the third unrolled iteration (on top of the balanced read split)
# baseline (speedup 1.0000x reference)
.Lgemm_T_loop:
	s_waitcnt lgkmcnt(0)
	s_add_u32 m0, s11, 0x1e080
	ds_read_b128 v[146:149], v164
	global_load_lds_dwordx4 v[220:221], off offset:-128
	v_mfma_f32_16x16x32_f16 v[82:85], v[134:137], v[86:89], v[82:85]
	ds_read_b128 v[150:153], v164 offset:2048
	v_mfma_f32_16x16x32_f16 v[58:61], v[138:141], v[86:89], v[58:61]
	ds_read_b128 v[154:157], v164 offset:4096
	v_mfma_f32_16x16x32_f16 v[14:17], v[142:145], v[86:89], v[14:17]
	ds_read_b128 v[110:113], v160
	v_mfma_f32_16x16x32_f16 v[78:81], v[134:137], v[90:93], v[78:81]
	ds_read_b128 v[114:117], v160 offset:2048
	v_mfma_f32_16x16x32_f16 v[22:25], v[138:141], v[90:93], v[22:25]
	ds_read_b128 v[118:121], v160 offset:4096
	v_mfma_f32_16x16x32_f16 v[30:33], v[142:145], v[90:93], v[30:33]
	s_add_u32 m0, s11, 0x20080
	ds_read_b128 v[122:125], v160 offset:6144
	global_load_lds_dwordx4 v[224:225], off offset:-128
	v_mfma_f32_16x16x32_f16 v[74:77], v[134:137], v[94:97], v[74:77]
	ds_read_b128 v[126:129], v160 offset:8192
	v_mfma_f32_16x16x32_f16 v[18:21], v[138:141], v[94:97], v[18:21]
	ds_read_b128 v[130:133], v160 offset:10240
	v_mfma_f32_16x16x32_f16 v[26:29], v[142:145], v[94:97], v[26:29]
	v_mfma_f32_16x16x32_f16 v[70:73], v[134:137], v[98:101], v[70:73]
	v_mfma_f32_16x16x32_f16 v[46:49], v[138:141], v[98:101], v[46:49]
	v_mfma_f32_16x16x32_f16 v[240:243], v[142:145], v[98:101], v[240:243]
	s_add_u32 m0, s11, 0x22080
	s_nop 0
	global_load_lds_dwordx4 v[228:229], off offset:-128
	v_mfma_f32_16x16x32_f16 v[66:69], v[134:137], v[102:105], v[66:69]
	v_mfma_f32_16x16x32_f16 v[42:45], v[138:141], v[102:105], v[42:45]
	v_mfma_f32_16x16x32_f16 v[236:239], v[142:145], v[102:105], v[236:239]
	v_mfma_f32_16x16x32_f16 v[62:65], v[134:137], v[106:109], v[62:65]
	v_mfma_f32_16x16x32_f16 v[38:41], v[138:141], v[106:109], v[38:41]
	v_mfma_f32_16x16x32_f16 v[34:37], v[142:145], v[106:109], v[34:37]
	s_waitcnt vmcnt(6) lgkmcnt(0)
	s_barrier
	s_add_u32 m0, s11, 0x0
	ds_read_b128 v[134:137], v162 offset:49152
	global_load_lds_dwordx4 v[218:219], off
	v_mfma_f32_16x16x32_f16 v[82:85], v[146:149], v[110:113], v[82:85]
	ds_read_b128 v[138:141], v162 offset:51200
	v_mfma_f32_16x16x32_f16 v[58:61], v[150:153], v[110:113], v[58:61]
	ds_read_b128 v[142:145], v162 offset:53248
	v_mfma_f32_16x16x32_f16 v[14:17], v[154:157], v[110:113], v[14:17]
	ds_read_b128 v[86:89], v158 offset:49152
	v_mfma_f32_16x16x32_f16 v[78:81], v[146:149], v[114:117], v[78:81]
	ds_read_b128 v[90:93], v158 offset:51200
	v_mfma_f32_16x16x32_f16 v[22:25], v[150:153], v[114:117], v[22:25]
	ds_read_b128 v[94:97], v158 offset:53248
	v_mfma_f32_16x16x32_f16 v[30:33], v[154:157], v[114:117], v[30:33]
	s_add_u32 m0, s11, 0x2000
	ds_read_b128 v[98:101], v158 offset:55296
	global_load_lds_dwordx4 v[222:223], off
	v_mfma_f32_16x16x32_f16 v[74:77], v[146:149], v[118:121], v[74:77]
	ds_read_b128 v[102:105], v158 offset:57344
	v_mfma_f32_16x16x32_f16 v[18:21], v[150:153], v[118:121], v[18:21]
	ds_read_b128 v[106:109], v158 offset:59392
	v_mfma_f32_16x16x32_f16 v[26:29], v[154:157], v[118:121], v[26:29]
	v_mfma_f32_16x16x32_f16 v[70:73], v[146:149], v[122:125], v[70:73]
	v_mfma_f32_16x16x32_f16 v[46:49], v[150:153], v[122:125], v[46:49]
	v_mfma_f32_16x16x32_f16 v[240:243], v[154:157], v[122:125], v[240:243]
	s_add_u32 m0, s11, 0x4000
	s_nop 0
	global_load_lds_dwordx4 v[226:227], off
	v_mfma_f32_16x16x32_f16 v[66:69], v[146:149], v[126:129], v[66:69]
	v_mfma_f32_16x16x32_f16 v[42:45], v[150:153], v[126:129], v[42:45]
	v_mfma_f32_16x16x32_f16 v[236:239], v[154:157], v[126:129], v[236:239]
	v_mfma_f32_16x16x32_f16 v[62:65], v[146:149], v[130:133], v[62:65]
	v_mfma_f32_16x16x32_f16 v[38:41], v[150:153], v[130:133], v[38:41]
	v_mfma_f32_16x16x32_f16 v[34:37], v[154:157], v[130:133], v[34:37]
	s_waitcnt lgkmcnt(0)
	s_add_u32 m0, s11, 0x6000
	ds_read_b128 v[146:149], v164 offset:49152
	global_load_lds_dwordx4 v[220:221], off
	v_mfma_f32_16x16x32_f16 v[82:85], v[134:137], v[86:89], v[82:85]
	ds_read_b128 v[150:153], v164 offset:51200
	v_mfma_f32_16x16x32_f16 v[58:61], v[138:141], v[86:89], v[58:61]
	ds_read_b128 v[154:157], v164 offset:53248
	v_mfma_f32_16x16x32_f16 v[14:17], v[142:145], v[86:89], v[14:17]
	ds_read_b128 v[110:113], v160 offset:49152
	v_mfma_f32_16x16x32_f16 v[78:81], v[134:137], v[90:93], v[78:81]
	ds_read_b128 v[114:117], v160 offset:51200
	v_mfma_f32_16x16x32_f16 v[22:25], v[138:141], v[90:93], v[22:25]
	ds_read_b128 v[118:121], v160 offset:53248
	v_mfma_f32_16x16x32_f16 v[30:33], v[142:145], v[90:93], v[30:33]
	s_add_u32 m0, s11, 0x8000
	ds_read_b128 v[122:125], v160 offset:55296
	global_load_lds_dwordx4 v[224:225], off
	v_mfma_f32_16x16x32_f16 v[74:77], v[134:137], v[94:97], v[74:77]
	ds_read_b128 v[126:129], v160 offset:57344
	v_mfma_f32_16x16x32_f16 v[18:21], v[138:141], v[94:97], v[18:21]
	ds_read_b128 v[130:133], v160 offset:59392
	v_mfma_f32_16x16x32_f16 v[26:29], v[142:145], v[94:97], v[26:29]
	v_mfma_f32_16x16x32_f16 v[70:73], v[134:137], v[98:101], v[70:73]
	v_mfma_f32_16x16x32_f16 v[46:49], v[138:141], v[98:101], v[46:49]
	v_mfma_f32_16x16x32_f16 v[240:243], v[142:145], v[98:101], v[240:243]
	s_add_u32 m0, s11, 0xa000
	s_nop 0
	global_load_lds_dwordx4 v[228:229], off
	v_mfma_f32_16x16x32_f16 v[66:69], v[134:137], v[102:105], v[66:69]
	v_mfma_f32_16x16x32_f16 v[42:45], v[138:141], v[102:105], v[42:45]
	v_mfma_f32_16x16x32_f16 v[236:239], v[142:145], v[102:105], v[236:239]
	v_mfma_f32_16x16x32_f16 v[62:65], v[134:137], v[106:109], v[62:65]
	v_mfma_f32_16x16x32_f16 v[38:41], v[138:141], v[106:109], v[38:41]
	v_mfma_f32_16x16x32_f16 v[34:37], v[142:145], v[106:109], v[34:37]
	s_waitcnt vmcnt(6) lgkmcnt(0)
	s_barrier
	s_add_u32 m0, s11, 0xbf80
	ds_read_b128 v[134:137], v163
	global_load_lds_dwordx4 v[218:219], off offset:128
	v_mfma_f32_16x16x32_f16 v[82:85], v[146:149], v[110:113], v[82:85]
	ds_read_b128 v[138:141], v163 offset:2048
	v_mfma_f32_16x16x32_f16 v[58:61], v[150:153], v[110:113], v[58:61]
	ds_read_b128 v[142:145], v163 offset:4096
	v_mfma_f32_16x16x32_f16 v[14:17], v[154:157], v[110:113], v[14:17]
	ds_read_b128 v[86:89], v159
	v_mfma_f32_16x16x32_f16 v[78:81], v[146:149], v[114:117], v[78:81]
	ds_read_b128 v[90:93], v159 offset:2048
	v_mfma_f32_16x16x32_f16 v[22:25], v[150:153], v[114:117], v[22:25]
	ds_read_b128 v[94:97], v159 offset:4096
	v_mfma_f32_16x16x32_f16 v[30:33], v[154:157], v[114:117], v[30:33]
	s_add_u32 m0, s11, 0xdf80
	ds_read_b128 v[98:101], v159 offset:6144
	global_load_lds_dwordx4 v[222:223], off offset:128
	v_mfma_f32_16x16x32_f16 v[74:77], v[146:149], v[118:121], v[74:77]
	ds_read_b128 v[102:105], v159 offset:8192
	v_mfma_f32_16x16x32_f16 v[18:21], v[150:153], v[118:121], v[18:21]
	ds_read_b128 v[106:109], v159 offset:10240
	v_mfma_f32_16x16x32_f16 v[26:29], v[154:157], v[118:121], v[26:29]
	v_mfma_f32_16x16x32_f16 v[70:73], v[146:149], v[122:125], v[70:73]
	v_mfma_f32_16x16x32_f16 v[46:49], v[150:153], v[122:125], v[46:49]
	v_mfma_f32_16x16x32_f16 v[240:243], v[154:157], v[122:125], v[240:243]
	s_add_u32 m0, s11, 0xff80
	s_nop 0
	global_load_lds_dwordx4 v[226:227], off offset:128
	v_mfma_f32_16x16x32_f16 v[66:69], v[146:149], v[126:129], v[66:69]
	v_mfma_f32_16x16x32_f16 v[42:45], v[150:153], v[126:129], v[42:45]
	v_mfma_f32_16x16x32_f16 v[236:239], v[154:157], v[126:129], v[236:239]
	v_mfma_f32_16x16x32_f16 v[62:65], v[146:149], v[130:133], v[62:65]
	v_mfma_f32_16x16x32_f16 v[38:41], v[150:153], v[130:133], v[38:41]
	v_mfma_f32_16x16x32_f16 v[34:37], v[154:157], v[130:133], v[34:37]
	s_waitcnt lgkmcnt(0)
	s_add_u32 m0, s11, 0x11f80
	ds_read_b128 v[146:149], v165
	global_load_lds_dwordx4 v[220:221], off offset:128
	v_mfma_f32_16x16x32_f16 v[82:85], v[134:137], v[86:89], v[82:85]
	ds_read_b128 v[150:153], v165 offset:2048
	v_mfma_f32_16x16x32_f16 v[58:61], v[138:141], v[86:89], v[58:61]
	ds_read_b128 v[154:157], v165 offset:4096
	v_mfma_f32_16x16x32_f16 v[14:17], v[142:145], v[86:89], v[14:17]
	ds_read_b128 v[110:113], v161
	v_mfma_f32_16x16x32_f16 v[78:81], v[134:137], v[90:93], v[78:81]
	ds_read_b128 v[114:117], v161 offset:2048
	v_mfma_f32_16x16x32_f16 v[22:25], v[138:141], v[90:93], v[22:25]
	ds_read_b128 v[118:121], v161 offset:4096
	v_mfma_f32_16x16x32_f16 v[30:33], v[142:145], v[90:93], v[30:33]
	s_add_u32 m0, s11, 0x13f80
	ds_read_b128 v[122:125], v161 offset:6144
	global_load_lds_dwordx4 v[224:225], off offset:128
	v_mfma_f32_16x16x32_f16 v[74:77], v[134:137], v[94:97], v[74:77]
	ds_read_b128 v[126:129], v161 offset:8192
	v_mfma_f32_16x16x32_f16 v[18:21], v[138:141], v[94:97], v[18:21]
	ds_read_b128 v[130:133], v161 offset:10240
	v_mfma_f32_16x16x32_f16 v[26:29], v[142:145], v[94:97], v[26:29]
	v_mfma_f32_16x16x32_f16 v[70:73], v[134:137], v[98:101], v[70:73]
	v_mfma_f32_16x16x32_f16 v[46:49], v[138:141], v[98:101], v[46:49]
	v_mfma_f32_16x16x32_f16 v[240:243], v[142:145], v[98:101], v[240:243]
	s_add_u32 m0, s11, 0x15f80
	s_nop 0
	global_load_lds_dwordx4 v[228:229], off offset:128
	v_mfma_f32_16x16x32_f16 v[66:69], v[134:137], v[102:105], v[66:69]
	v_mfma_f32_16x16x32_f16 v[42:45], v[138:141], v[102:105], v[42:45]
	v_mfma_f32_16x16x32_f16 v[236:239], v[142:145], v[102:105], v[236:239]
	v_mfma_f32_16x16x32_f16 v[62:65], v[134:137], v[106:109], v[62:65]
	v_mfma_f32_16x16x32_f16 v[38:41], v[138:141], v[106:109], v[38:41]
	v_mfma_f32_16x16x32_f16 v[34:37], v[142:145], v[106:109], v[34:37]
	s_waitcnt vmcnt(6) lgkmcnt(0)
	s_barrier
	s_add_u32 m0, s11, 0x17f00
	ds_read_b128 v[134:137], v162
	global_load_lds_dwordx4 v[218:219], off offset:256
	v_mfma_f32_16x16x32_f16 v[82:85], v[146:149], v[110:113], v[82:85]
	ds_read_b128 v[138:141], v162 offset:2048
	v_mfma_f32_16x16x32_f16 v[58:61], v[150:153], v[110:113], v[58:61]
	ds_read_b128 v[142:145], v162 offset:4096
	v_mfma_f32_16x16x32_f16 v[14:17], v[154:157], v[110:113], v[14:17]
	ds_read_b128 v[86:89], v158
	v_mfma_f32_16x16x32_f16 v[78:81], v[146:149], v[114:117], v[78:81]
	ds_read_b128 v[90:93], v158 offset:2048
	v_mfma_f32_16x16x32_f16 v[22:25], v[150:153], v[114:117], v[22:25]
	ds_read_b128 v[94:97], v158 offset:4096
	v_mfma_f32_16x16x32_f16 v[30:33], v[154:157], v[114:117], v[30:33]
	s_add_u32 m0, s11, 0x19f00
	ds_read_b128 v[98:101], v158 offset:6144
	global_load_lds_dwordx4 v[222:223], off offset:256
	v_mfma_f32_16x16x32_f16 v[74:77], v[146:149], v[118:121], v[74:77]
	ds_read_b128 v[102:105], v158 offset:8192
	v_mfma_f32_16x16x32_f16 v[18:21], v[150:153], v[118:121], v[18:21]
	ds_read_b128 v[106:109], v158 offset:10240
	v_mfma_f32_16x16x32_f16 v[26:29], v[154:157], v[118:121], v[26:29]
	v_mfma_f32_16x16x32_f16 v[70:73], v[146:149], v[122:125], v[70:73]
	v_lshl_add_u64 v[220:221], v[220:221], 0, s[20:21]
	v_mfma_f32_16x16x32_f16 v[46:49], v[150:153], v[122:125], v[46:49]
	v_lshl_add_u64 v[224:225], v[224:225], 0, s[20:21]
	v_mfma_f32_16x16x32_f16 v[240:243], v[154:157], v[122:125], v[240:243]
	s_add_u32 m0, s11, 0x1bf00
	s_nop 0
	global_load_lds_dwordx4 v[226:227], off offset:256
	v_mfma_f32_16x16x32_f16 v[66:69], v[146:149], v[126:129], v[66:69]
	v_lshl_add_u64 v[228:229], v[228:229], 0, s[20:21]
	v_mfma_f32_16x16x32_f16 v[42:45], v[150:153], v[126:129], v[42:45]
	v_lshl_add_u64 v[218:219], v[218:219], 0, s[20:21]
	v_mfma_f32_16x16x32_f16 v[236:239], v[154:157], v[126:129], v[236:239]
	v_lshl_add_u64 v[222:223], v[222:223], 0, s[20:21]
	v_mfma_f32_16x16x32_f16 v[62:65], v[146:149], v[130:133], v[62:65]
	v_lshl_add_u64 v[226:227], v[226:227], 0, s[20:21]
	v_mfma_f32_16x16x32_f16 v[38:41], v[150:153], v[130:133], v[38:41]
	v_mfma_f32_16x16x32_f16 v[34:37], v[154:157], v[130:133], v[34:37]
	s_sub_u32 s22, s22, 1
	s_cmp_lg_u32 s22, 0
	s_cbranch_scc1 .Lgemm_T_loop
	s_waitcnt lgkmcnt(0)
	s_add_u32 m0, s11, 0x1e080
	ds_read_b128 v[146:149], v164
	global_load_lds_dwordx4 v[220:221], off offset:-128
	v_mfma_f32_16x16x32_f16 v[82:85], v[134:137], v[86:89], v[82:85]
	ds_read_b128 v[150:153], v164 offset:2048
	v_mfma_f32_16x16x32_f16 v[58:61], v[138:141], v[86:89], v[58:61]
	ds_read_b128 v[154:157], v164 offset:4096
	v_mfma_f32_16x16x32_f16 v[14:17], v[142:145], v[86:89], v[14:17]
	ds_read_b128 v[110:113], v160
	v_mfma_f32_16x16x32_f16 v[78:81], v[134:137], v[90:93], v[78:81]
	ds_read_b128 v[114:117], v160 offset:2048
	v_mfma_f32_16x16x32_f16 v[22:25], v[138:141], v[90:93], v[22:25]
	ds_read_b128 v[118:121], v160 offset:4096
	v_mfma_f32_16x16x32_f16 v[30:33], v[142:145], v[90:93], v[30:33]
	s_add_u32 m0, s11, 0x20080
	ds_read_b128 v[122:125], v160 offset:6144
	global_load_lds_dwordx4 v[224:225], off offset:-128
	v_mfma_f32_16x16x32_f16 v[74:77], v[134:137], v[94:97], v[74:77]
	ds_read_b128 v[126:129], v160 offset:8192
	v_mfma_f32_16x16x32_f16 v[18:21], v[138:141], v[94:97], v[18:21]
	ds_read_b128 v[130:133], v160 offset:10240
	v_mfma_f32_16x16x32_f16 v[26:29], v[142:145], v[94:97], v[26:29]
	v_mfma_f32_16x16x32_f16 v[70:73], v[134:137], v[98:101], v[70:73]
	v_mfma_f32_16x16x32_f16 v[46:49], v[138:141], v[98:101], v[46:49]
	v_mfma_f32_16x16x32_f16 v[240:243], v[142:145], v[98:101], v[240:243]
	s_add_u32 m0, s11, 0x22080
	s_nop 0
	global_load_lds_dwordx4 v[228:229], off offset:-128
	v_mfma_f32_16x16x32_f16 v[66:69], v[134:137], v[102:105], v[66:69]
	v_mfma_f32_16x16x32_f16 v[42:45], v[138:141], v[102:105], v[42:45]
	v_mfma_f32_16x16x32_f16 v[236:239], v[142:145], v[102:105], v[236:239]
	v_mfma_f32_16x16x32_f16 v[62:65], v[134:137], v[106:109], v[62:65]
	v_mfma_f32_16x16x32_f16 v[38:41], v[138:141], v[106:109], v[38:41]
	v_mfma_f32_16x16x32_f16 v[34:37], v[142:145], v[106:109], v[34:37]
	s_waitcnt vmcnt(6) lgkmcnt(0)
	s_barrier
	s_add_u32 m0, s11, 0x0
	ds_read_b128 v[134:137], v162 offset:49152
	global_load_lds_dwordx4 v[218:219], off
	v_mfma_f32_16x16x32_f16 v[82:85], v[146:149], v[110:113], v[82:85]
	ds_read_b128 v[138:141], v162 offset:51200
	v_mfma_f32_16x16x32_f16 v[58:61], v[150:153], v[110:113], v[58:61]
	ds_read_b128 v[142:145], v162 offset:53248
	v_mfma_f32_16x16x32_f16 v[14:17], v[154:157], v[110:113], v[14:17]
	ds_read_b128 v[86:89], v158 offset:49152
	v_mfma_f32_16x16x32_f16 v[78:81], v[146:149], v[114:117], v[78:81]
	ds_read_b128 v[90:93], v158 offset:51200
	v_mfma_f32_16x16x32_f16 v[22:25], v[150:153], v[114:117], v[22:25]
	ds_read_b128 v[94:97], v158 offset:53248
	v_mfma_f32_16x16x32_f16 v[30:33], v[154:157], v[114:117], v[30:33]
	s_add_u32 m0, s11, 0x2000
	ds_read_b128 v[98:101], v158 offset:55296
	global_load_lds_dwordx4 v[222:223], off
	v_mfma_f32_16x16x32_f16 v[74:77], v[146:149], v[118:121], v[74:77]
	ds_read_b128 v[102:105], v158 offset:57344
	v_mfma_f32_16x16x32_f16 v[18:21], v[150:153], v[118:121], v[18:21]
	ds_read_b128 v[106:109], v158 offset:59392
	v_mfma_f32_16x16x32_f16 v[26:29], v[154:157], v[118:121], v[26:29]
	v_mfma_f32_16x16x32_f16 v[70:73], v[146:149], v[122:125], v[70:73]
	v_mfma_f32_16x16x32_f16 v[46:49], v[150:153], v[122:125], v[46:49]
	v_mfma_f32_16x16x32_f16 v[240:243], v[154:157], v[122:125], v[240:243]
	s_add_u32 m0, s11, 0x4000
	s_nop 0
	global_load_lds_dwordx4 v[226:227], off
	v_mfma_f32_16x16x32_f16 v[66:69], v[146:149], v[126:129], v[66:69]
	v_mfma_f32_16x16x32_f16 v[42:45], v[150:153], v[126:129], v[42:45]
	v_mfma_f32_16x16x32_f16 v[236:239], v[154:157], v[126:129], v[236:239]
	v_mfma_f32_16x16x32_f16 v[62:65], v[146:149], v[130:133], v[62:65]
	v_mfma_f32_16x16x32_f16 v[38:41], v[150:153], v[130:133], v[38:41]
	v_mfma_f32_16x16x32_f16 v[34:37], v[154:157], v[130:133], v[34:37]
	s_waitcnt lgkmcnt(0)
	s_add_u32 m0, s11, 0x6000
	ds_read_b128 v[146:149], v164 offset:49152
	global_load_lds_dwordx4 v[220:221], off
	v_mfma_f32_16x16x32_f16 v[82:85], v[134:137], v[86:89], v[82:85]
	ds_read_b128 v[150:153], v164 offset:51200
	v_mfma_f32_16x16x32_f16 v[58:61], v[138:141], v[86:89], v[58:61]
	ds_read_b128 v[154:157], v164 offset:53248
	v_mfma_f32_16x16x32_f16 v[14:17], v[142:145], v[86:89], v[14:17]
	ds_read_b128 v[110:113], v160 offset:49152
	v_mfma_f32_16x16x32_f16 v[78:81], v[134:137], v[90:93], v[78:81]
	ds_read_b128 v[114:117], v160 offset:51200
	v_mfma_f32_16x16x32_f16 v[22:25], v[138:141], v[90:93], v[22:25]
	ds_read_b128 v[118:121], v160 offset:53248
	v_mfma_f32_16x16x32_f16 v[30:33], v[142:145], v[90:93], v[30:33]
	s_add_u32 m0, s11, 0x8000
	ds_read_b128 v[122:125], v160 offset:55296
	global_load_lds_dwordx4 v[224:225], off
	v_mfma_f32_16x16x32_f16 v[74:77], v[134:137], v[94:97], v[74:77]
	ds_read_b128 v[126:129], v160 offset:57344
	v_mfma_f32_16x16x32_f16 v[18:21], v[138:141], v[94:97], v[18:21]
	ds_read_b128 v[130:133], v160 offset:59392
	v_mfma_f32_16x16x32_f16 v[26:29], v[142:145], v[94:97], v[26:29]
	v_mfma_f32_16x16x32_f16 v[70:73], v[134:137], v[98:101], v[70:73]
	v_mfma_f32_16x16x32_f16 v[46:49], v[138:141], v[98:101], v[46:49]
	v_mfma_f32_16x16x32_f16 v[240:243], v[142:145], v[98:101], v[240:243]
	s_add_u32 m0, s11, 0xa000
	s_nop 0
	global_load_lds_dwordx4 v[228:229], off
	v_mfma_f32_16x16x32_f16 v[66:69], v[134:137], v[102:105], v[66:69]
	v_mfma_f32_16x16x32_f16 v[42:45], v[138:141], v[102:105], v[42:45]
	v_mfma_f32_16x16x32_f16 v[236:239], v[142:145], v[102:105], v[236:239]
	v_mfma_f32_16x16x32_f16 v[62:65], v[134:137], v[106:109], v[62:65]
	v_mfma_f32_16x16x32_f16 v[38:41], v[138:141], v[106:109], v[38:41]
	v_mfma_f32_16x16x32_f16 v[34:37], v[142:145], v[106:109], v[34:37]
	s_waitcnt vmcnt(6) lgkmcnt(0)
	s_barrier
	s_lshl_b32 s26, s17, 2
	s_add_u32 s26, s24, s26
	s_addc_u32 s27, s25, 0
	v_lshlrev_b32_e32 v50, 4, v231
	global_load_dwordx4 v[10:13], v50, s[26:27]
	global_load_dwordx4 v[6:9], v50, s[26:27] offset:64
	global_load_dwordx4 v[2:5], v50, s[26:27] offset:128
	ds_read_b128 v[134:137], v163
	v_mfma_f32_16x16x32_f16 v[82:85], v[146:149], v[110:113], v[82:85]
	ds_read_b128 v[138:141], v163 offset:2048
	v_mfma_f32_16x16x32_f16 v[58:61], v[150:153], v[110:113], v[58:61]
	ds_read_b128 v[142:145], v163 offset:4096
	v_mfma_f32_16x16x32_f16 v[14:17], v[154:157], v[110:113], v[14:17]
	ds_read_b128 v[86:89], v159
	v_mfma_f32_16x16x32_f16 v[78:81], v[146:149], v[114:117], v[78:81]
	ds_read_b128 v[90:93], v159 offset:2048
	v_mfma_f32_16x16x32_f16 v[22:25], v[150:153], v[114:117], v[22:25]
	ds_read_b128 v[94:97], v159 offset:4096
	v_mfma_f32_16x16x32_f16 v[30:33], v[154:157], v[114:117], v[30:33]
	ds_read_b128 v[98:101], v159 offset:6144
	v_mfma_f32_16x16x32_f16 v[74:77], v[146:149], v[118:121], v[74:77]
	ds_read_b128 v[102:105], v159 offset:8192
	v_mfma_f32_16x16x32_f16 v[18:21], v[150:153], v[118:121], v[18:21]
	ds_read_b128 v[106:109], v159 offset:10240
	v_mfma_f32_16x16x32_f16 v[26:29], v[154:157], v[118:121], v[26:29]
	v_mfma_f32_16x16x32_f16 v[70:73], v[146:149], v[122:125], v[70:73]
	v_mfma_f32_16x16x32_f16 v[46:49], v[150:153], v[122:125], v[46:49]
	v_mfma_f32_16x16x32_f16 v[240:243], v[154:157], v[122:125], v[240:243]
	v_mfma_f32_16x16x32_f16 v[66:69], v[146:149], v[126:129], v[66:69]
	v_mfma_f32_16x16x32_f16 v[42:45], v[150:153], v[126:129], v[42:45]
	v_mfma_f32_16x16x32_f16 v[236:239], v[154:157], v[126:129], v[236:239]
	v_mfma_f32_16x16x32_f16 v[62:65], v[146:149], v[130:133], v[62:65]
	v_mfma_f32_16x16x32_f16 v[38:41], v[150:153], v[130:133], v[38:41]
	v_mfma_f32_16x16x32_f16 v[34:37], v[154:157], v[130:133], v[34:37]
	s_waitcnt lgkmcnt(0)
	ds_read_b128 v[146:149], v165
	v_mfma_f32_16x16x32_f16 v[82:85], v[134:137], v[86:89], v[82:85]
	ds_read_b128 v[150:153], v165 offset:2048
	v_mfma_f32_16x16x32_f16 v[58:61], v[138:141], v[86:89], v[58:61]
	ds_read_b128 v[154:157], v165 offset:4096
	v_mfma_f32_16x16x32_f16 v[14:17], v[142:145], v[86:89], v[14:17]
	ds_read_b128 v[110:113], v161
	v_mfma_f32_16x16x32_f16 v[78:81], v[134:137], v[90:93], v[78:81]
	ds_read_b128 v[114:117], v161 offset:2048
	v_mfma_f32_16x16x32_f16 v[22:25], v[138:141], v[90:93], v[22:25]
	ds_read_b128 v[118:121], v161 offset:4096
	v_mfma_f32_16x16x32_f16 v[30:33], v[142:145], v[90:93], v[30:33]
	ds_read_b128 v[122:125], v161 offset:6144
	v_mfma_f32_16x16x32_f16 v[74:77], v[134:137], v[94:97], v[74:77]
	ds_read_b128 v[126:129], v161 offset:8192
	v_mfma_f32_16x16x32_f16 v[18:21], v[138:141], v[94:97], v[18:21]
	ds_read_b128 v[130:133], v161 offset:10240
	v_mfma_f32_16x16x32_f16 v[26:29], v[142:145], v[94:97], v[26:29]
	v_mfma_f32_16x16x32_f16 v[70:73], v[134:137], v[98:101], v[70:73]
	v_mfma_f32_16x16x32_f16 v[46:49], v[138:141], v[98:101], v[46:49]
	v_mfma_f32_16x16x32_f16 v[240:243], v[142:145], v[98:101], v[240:243]
	v_mfma_f32_16x16x32_f16 v[66:69], v[134:137], v[102:105], v[66:69]
	v_mfma_f32_16x16x32_f16 v[42:45], v[138:141], v[102:105], v[42:45]
	v_mfma_f32_16x16x32_f16 v[236:239], v[142:145], v[102:105], v[236:239]
	v_mfma_f32_16x16x32_f16 v[62:65], v[134:137], v[106:109], v[62:65]
	v_mfma_f32_16x16x32_f16 v[38:41], v[138:141], v[106:109], v[38:41]
	v_mfma_f32_16x16x32_f16 v[34:37], v[142:145], v[106:109], v[34:37]
	s_waitcnt vmcnt(3) lgkmcnt(0)
	s_barrier
	ds_read_b128 v[134:137], v162
	v_mfma_f32_16x16x32_f16 v[82:85], v[146:149], v[110:113], v[82:85]
	ds_read_b128 v[138:141], v162 offset:2048
	v_mfma_f32_16x16x32_f16 v[58:61], v[150:153], v[110:113], v[58:61]
	ds_read_b128 v[142:145], v162 offset:4096
	v_mfma_f32_16x16x32_f16 v[14:17], v[154:157], v[110:113], v[14:17]
	ds_read_b128 v[86:89], v158
	v_mfma_f32_16x16x32_f16 v[78:81], v[146:149], v[114:117], v[78:81]
	ds_read_b128 v[90:93], v158 offset:2048
	v_mfma_f32_16x16x32_f16 v[22:25], v[150:153], v[114:117], v[22:25]
	ds_read_b128 v[94:97], v158 offset:4096
	v_mfma_f32_16x16x32_f16 v[30:33], v[154:157], v[114:117], v[30:33]
	ds_read_b128 v[98:101], v158 offset:6144
	v_mfma_f32_16x16x32_f16 v[74:77], v[146:149], v[118:121], v[74:77]
	ds_read_b128 v[102:105], v158 offset:8192
	v_mfma_f32_16x16x32_f16 v[18:21], v[150:153], v[118:121], v[18:21]
	ds_read_b128 v[106:109], v158 offset:10240
	v_mfma_f32_16x16x32_f16 v[26:29], v[154:157], v[118:121], v[26:29]
	v_mfma_f32_16x16x32_f16 v[70:73], v[146:149], v[122:125], v[70:73]
	v_mfma_f32_16x16x32_f16 v[46:49], v[150:153], v[122:125], v[46:49]
	v_mfma_f32_16x16x32_f16 v[240:243], v[154:157], v[122:125], v[240:243]
	v_mfma_f32_16x16x32_f16 v[66:69], v[146:149], v[126:129], v[66:69]
	v_mfma_f32_16x16x32_f16 v[42:45], v[150:153], v[126:129], v[42:45]
	v_mfma_f32_16x16x32_f16 v[236:239], v[154:157], v[126:129], v[236:239]
	v_mfma_f32_16x16x32_f16 v[62:65], v[146:149], v[130:133], v[62:65]
	v_mfma_f32_16x16x32_f16 v[38:41], v[150:153], v[130:133], v[38:41]
	v_mfma_f32_16x16x32_f16 v[34:37], v[154:157], v[130:133], v[34:37]
	s_waitcnt lgkmcnt(0)
	ds_read_b128 v[146:149], v164
	v_mfma_f32_16x16x32_f16 v[82:85], v[134:137], v[86:89], v[82:85]
	ds_read_b128 v[150:153], v164 offset:2048
	v_mfma_f32_16x16x32_f16 v[58:61], v[138:141], v[86:89], v[58:61]
	ds_read_b128 v[154:157], v164 offset:4096
	v_mfma_f32_16x16x32_f16 v[14:17], v[142:145], v[86:89], v[14:17]
	ds_read_b128 v[110:113], v160
	v_mfma_f32_16x16x32_f16 v[78:81], v[134:137], v[90:93], v[78:81]
	ds_read_b128 v[114:117], v160 offset:2048
	v_mfma_f32_16x16x32_f16 v[22:25], v[138:141], v[90:93], v[22:25]
	ds_read_b128 v[118:121], v160 offset:4096
	v_mfma_f32_16x16x32_f16 v[30:33], v[142:145], v[90:93], v[30:33]
	ds_read_b128 v[122:125], v160 offset:6144
	v_mfma_f32_16x16x32_f16 v[74:77], v[134:137], v[94:97], v[74:77]
	ds_read_b128 v[126:129], v160 offset:8192
	v_mfma_f32_16x16x32_f16 v[18:21], v[138:141], v[94:97], v[18:21]
	ds_read_b128 v[130:133], v160 offset:10240
	v_mfma_f32_16x16x32_f16 v[26:29], v[142:145], v[94:97], v[26:29]
	v_mfma_f32_16x16x32_f16 v[70:73], v[134:137], v[98:101], v[70:73]
	v_mfma_f32_16x16x32_f16 v[46:49], v[138:141], v[98:101], v[46:49]
	v_mfma_f32_16x16x32_f16 v[240:243], v[142:145], v[98:101], v[240:243]
	v_mfma_f32_16x16x32_f16 v[66:69], v[134:137], v[102:105], v[66:69]
	v_mfma_f32_16x16x32_f16 v[42:45], v[138:141], v[102:105], v[42:45]
	v_mfma_f32_16x16x32_f16 v[236:239], v[142:145], v[102:105], v[236:239]
	v_mfma_f32_16x16x32_f16 v[62:65], v[134:137], v[106:109], v[62:65]
	v_mfma_f32_16x16x32_f16 v[38:41], v[138:141], v[106:109], v[38:41]
	v_mfma_f32_16x16x32_f16 v[34:37], v[142:145], v[106:109], v[34:37]
	s_waitcnt lgkmcnt(0)
	v_mfma_f32_16x16x32_f16 v[82:85], v[146:149], v[110:113], v[82:85]
	v_mfma_f32_16x16x32_f16 v[58:61], v[150:153], v[110:113], v[58:61]
	v_mfma_f32_16x16x32_f16 v[14:17], v[154:157], v[110:113], v[14:17]
	v_mfma_f32_16x16x32_f16 v[78:81], v[146:149], v[114:117], v[78:81]
	v_mfma_f32_16x16x32_f16 v[22:25], v[150:153], v[114:117], v[22:25]
	v_mfma_f32_16x16x32_f16 v[30:33], v[154:157], v[114:117], v[30:33]
	v_mfma_f32_16x16x32_f16 v[74:77], v[146:149], v[118:121], v[74:77]
	v_mfma_f32_16x16x32_f16 v[18:21], v[150:153], v[118:121], v[18:21]
	v_mfma_f32_16x16x32_f16 v[26:29], v[154:157], v[118:121], v[26:29]
	v_mfma_f32_16x16x32_f16 v[70:73], v[146:149], v[122:125], v[70:73]
	v_mfma_f32_16x16x32_f16 v[46:49], v[150:153], v[122:125], v[46:49]
	v_mfma_f32_16x16x32_f16 v[240:243], v[154:157], v[122:125], v[240:243]
	v_mfma_f32_16x16x32_f16 v[66:69], v[146:149], v[126:129], v[66:69]
	v_mfma_f32_16x16x32_f16 v[42:45], v[150:153], v[126:129], v[42:45]
	v_mfma_f32_16x16x32_f16 v[236:239], v[154:157], v[126:129], v[236:239]
	v_mfma_f32_16x16x32_f16 v[62:65], v[146:149], v[130:133], v[62:65]
	v_mfma_f32_16x16x32_f16 v[38:41], v[150:153], v[130:133], v[38:41]
	v_mfma_f32_16x16x32_f16 v[34:37], v[154:157], v[130:133], v[34:37]
	s_branch .LBB1_76
.Lgemm_N_loop:
	s_waitcnt lgkmcnt(0)
	s_add_u32 m0, s11, 0x1e080
	ds_read_b128 v[146:149], v164
	global_load_lds_dwordx4 v[220:221], off offset:-128
	v_mfma_f32_16x16x32_f16 v[82:85], v[86:89], v[134:137], v[82:85]
	ds_read_b128 v[150:153], v164 offset:2048
	v_mfma_f32_16x16x32_f16 v[58:61], v[86:89], v[138:141], v[58:61]
	ds_read_b128 v[154:157], v164 offset:4096
	v_mfma_f32_16x16x32_f16 v[14:17], v[86:89], v[142:145], v[14:17]
	ds_read_b128 v[110:113], v160
	v_mfma_f32_16x16x32_f16 v[78:81], v[90:93], v[134:137], v[78:81]
	ds_read_b128 v[114:117], v160 offset:2048
	v_mfma_f32_16x16x32_f16 v[22:25], v[90:93], v[138:141], v[22:25]
	ds_read_b128 v[118:121], v160 offset:4096
	v_mfma_f32_16x16x32_f16 v[30:33], v[90:93], v[142:145], v[30:33]
	s_add_u32 m0, s11, 0x20080
	ds_read_b128 v[122:125], v160 offset:6144
	global_load_lds_dwordx4 v[224:225], off offset:-128
	v_mfma_f32_16x16x32_f16 v[74:77], v[94:97], v[134:137], v[74:77]
	ds_read_b128 v[126:129], v160 offset:8192
	v_mfma_f32_16x16x32_f16 v[18:21], v[94:97], v[138:141], v[18:21]
	ds_read_b128 v[130:133], v160 offset:10240
	v_mfma_f32_16x16x32_f16 v[26:29], v[94:97], v[142:145], v[26:29]
	v_mfma_f32_16x16x32_f16 v[70:73], v[98:101], v[134:137], v[70:73]
	v_mfma_f32_16x16x32_f16 v[46:49], v[98:101], v[138:141], v[46:49]
	v_mfma_f32_16x16x32_f16 v[240:243], v[98:101], v[142:145], v[240:243]
	s_add_u32 m0, s11, 0x22080
	s_nop 0
	global_load_lds_dwordx4 v[228:229], off offset:-128
	v_mfma_f32_16x16x32_f16 v[66:69], v[102:105], v[134:137], v[66:69]
	v_mfma_f32_16x16x32_f16 v[42:45], v[102:105], v[138:141], v[42:45]
	v_mfma_f32_16x16x32_f16 v[236:239], v[102:105], v[142:145], v[236:239]
	v_mfma_f32_16x16x32_f16 v[62:65], v[106:109], v[134:137], v[62:65]
	v_mfma_f32_16x16x32_f16 v[38:41], v[106:109], v[138:141], v[38:41]
	v_mfma_f32_16x16x32_f16 v[34:37], v[106:109], v[142:145], v[34:37]
	s_waitcnt vmcnt(6) lgkmcnt(0)
	s_barrier
	s_add_u32 m0, s11, 0x0
	ds_read_b128 v[134:137], v162 offset:49152
	global_load_lds_dwordx4 v[218:219], off
	v_mfma_f32_16x16x32_f16 v[82:85], v[110:113], v[146:149], v[82:85]
	ds_read_b128 v[138:141], v162 offset:51200
	v_mfma_f32_16x16x32_f16 v[58:61], v[110:113], v[150:153], v[58:61]
	ds_read_b128 v[142:145], v162 offset:53248
	v_mfma_f32_16x16x32_f16 v[14:17], v[110:113], v[154:157], v[14:17]
	ds_read_b128 v[86:89], v158 offset:49152
	v_mfma_f32_16x16x32_f16 v[78:81], v[114:117], v[146:149], v[78:81]
	ds_read_b128 v[90:93], v158 offset:51200
	v_mfma_f32_16x16x32_f16 v[22:25], v[114:117], v[150:153], v[22:25]
	ds_read_b128 v[94:97], v158 offset:53248
	v_mfma_f32_16x16x32_f16 v[30:33], v[114:117], v[154:157], v[30:33]
	s_add_u32 m0, s11, 0x2000
	ds_read_b128 v[98:101], v158 offset:55296
	global_load_lds_dwordx4 v[222:223], off
	v_mfma_f32_16x16x32_f16 v[74:77], v[118:121], v[146:149], v[74:77]
	ds_read_b128 v[102:105], v158 offset:57344
	v_mfma_f32_16x16x32_f16 v[18:21], v[118:121], v[150:153], v[18:21]
	ds_read_b128 v[106:109], v158 offset:59392
	v_mfma_f32_16x16x32_f16 v[26:29], v[118:121], v[154:157], v[26:29]
	v_mfma_f32_16x16x32_f16 v[70:73], v[122:125], v[146:149], v[70:73]
	v_mfma_f32_16x16x32_f16 v[46:49], v[122:125], v[150:153], v[46:49]
	v_mfma_f32_16x16x32_f16 v[240:243], v[122:125], v[154:157], v[240:243]
	s_add_u32 m0, s11, 0x4000
	s_nop 0
	global_load_lds_dwordx4 v[226:227], off
	v_mfma_f32_16x16x32_f16 v[66:69], v[126:129], v[146:149], v[66:69]
	v_mfma_f32_16x16x32_f16 v[42:45], v[126:129], v[150:153], v[42:45]
	v_mfma_f32_16x16x32_f16 v[236:239], v[126:129], v[154:157], v[236:239]
	v_mfma_f32_16x16x32_f16 v[62:65], v[130:133], v[146:149], v[62:65]
	v_mfma_f32_16x16x32_f16 v[38:41], v[130:133], v[150:153], v[38:41]
	v_mfma_f32_16x16x32_f16 v[34:37], v[130:133], v[154:157], v[34:37]
	s_waitcnt lgkmcnt(0)
	s_add_u32 m0, s11, 0x6000
	ds_read_b128 v[146:149], v164 offset:49152
	global_load_lds_dwordx4 v[220:221], off
	v_mfma_f32_16x16x32_f16 v[82:85], v[86:89], v[134:137], v[82:85]
	ds_read_b128 v[150:153], v164 offset:51200
	v_mfma_f32_16x16x32_f16 v[58:61], v[86:89], v[138:141], v[58:61]
	ds_read_b128 v[154:157], v164 offset:53248
	v_mfma_f32_16x16x32_f16 v[14:17], v[86:89], v[142:145], v[14:17]
	ds_read_b128 v[110:113], v160 offset:49152
	v_mfma_f32_16x16x32_f16 v[78:81], v[90:93], v[134:137], v[78:81]
	ds_read_b128 v[114:117], v160 offset:51200
	v_mfma_f32_16x16x32_f16 v[22:25], v[90:93], v[138:141], v[22:25]
	ds_read_b128 v[118:121], v160 offset:53248
	v_mfma_f32_16x16x32_f16 v[30:33], v[90:93], v[142:145], v[30:33]
	s_add_u32 m0, s11, 0x8000
	ds_read_b128 v[122:125], v160 offset:55296
	global_load_lds_dwordx4 v[224:225], off
	v_mfma_f32_16x16x32_f16 v[74:77], v[94:97], v[134:137], v[74:77]
	ds_read_b128 v[126:129], v160 offset:57344
	v_mfma_f32_16x16x32_f16 v[18:21], v[94:97], v[138:141], v[18:21]
	ds_read_b128 v[130:133], v160 offset:59392
	v_mfma_f32_16x16x32_f16 v[26:29], v[94:97], v[142:145], v[26:29]
	v_mfma_f32_16x16x32_f16 v[70:73], v[98:101], v[134:137], v[70:73]
	v_mfma_f32_16x16x32_f16 v[46:49], v[98:101], v[138:141], v[46:49]
	v_mfma_f32_16x16x32_f16 v[240:243], v[98:101], v[142:145], v[240:243]
	s_add_u32 m0, s11, 0xa000
	s_nop 0
	global_load_lds_dwordx4 v[228:229], off
	v_mfma_f32_16x16x32_f16 v[66:69], v[102:105], v[134:137], v[66:69]
	v_mfma_f32_16x16x32_f16 v[42:45], v[102:105], v[138:141], v[42:45]
	v_mfma_f32_16x16x32_f16 v[236:239], v[102:105], v[142:145], v[236:239]
	v_mfma_f32_16x16x32_f16 v[62:65], v[106:109], v[134:137], v[62:65]
	v_mfma_f32_16x16x32_f16 v[38:41], v[106:109], v[138:141], v[38:41]
	v_mfma_f32_16x16x32_f16 v[34:37], v[106:109], v[142:145], v[34:37]
	s_waitcnt vmcnt(6) lgkmcnt(0)
	s_barrier
	s_add_u32 m0, s11, 0xbf80
	ds_read_b128 v[134:137], v163
	global_load_lds_dwordx4 v[218:219], off offset:128
	v_mfma_f32_16x16x32_f16 v[82:85], v[110:113], v[146:149], v[82:85]
	ds_read_b128 v[138:141], v163 offset:2048
	v_mfma_f32_16x16x32_f16 v[58:61], v[110:113], v[150:153], v[58:61]
	ds_read_b128 v[142:145], v163 offset:4096
	v_mfma_f32_16x16x32_f16 v[14:17], v[110:113], v[154:157], v[14:17]
	ds_read_b128 v[86:89], v159
	v_mfma_f32_16x16x32_f16 v[78:81], v[114:117], v[146:149], v[78:81]
	ds_read_b128 v[90:93], v159 offset:2048
	v_mfma_f32_16x16x32_f16 v[22:25], v[114:117], v[150:153], v[22:25]
	ds_read_b128 v[94:97], v159 offset:4096
	v_mfma_f32_16x16x32_f16 v[30:33], v[114:117], v[154:157], v[30:33]
	s_add_u32 m0, s11, 0xdf80
	ds_read_b128 v[98:101], v159 offset:6144
	global_load_lds_dwordx4 v[222:223], off offset:128
	v_mfma_f32_16x16x32_f16 v[74:77], v[118:121], v[146:149], v[74:77]
	ds_read_b128 v[102:105], v159 offset:8192
	v_mfma_f32_16x16x32_f16 v[18:21], v[118:121], v[150:153], v[18:21]
	ds_read_b128 v[106:109], v159 offset:10240
	v_mfma_f32_16x16x32_f16 v[26:29], v[118:121], v[154:157], v[26:29]
	v_mfma_f32_16x16x32_f16 v[70:73], v[122:125], v[146:149], v[70:73]
	v_mfma_f32_16x16x32_f16 v[46:49], v[122:125], v[150:153], v[46:49]
	v_mfma_f32_16x16x32_f16 v[240:243], v[122:125], v[154:157], v[240:243]
	s_add_u32 m0, s11, 0xff80
	s_nop 0
	global_load_lds_dwordx4 v[226:227], off offset:128
	v_mfma_f32_16x16x32_f16 v[66:69], v[126:129], v[146:149], v[66:69]
	v_mfma_f32_16x16x32_f16 v[42:45], v[126:129], v[150:153], v[42:45]
	v_mfma_f32_16x16x32_f16 v[236:239], v[126:129], v[154:157], v[236:239]
	v_mfma_f32_16x16x32_f16 v[62:65], v[130:133], v[146:149], v[62:65]
	v_mfma_f32_16x16x32_f16 v[38:41], v[130:133], v[150:153], v[38:41]
	v_mfma_f32_16x16x32_f16 v[34:37], v[130:133], v[154:157], v[34:37]
	s_waitcnt lgkmcnt(0)
	s_add_u32 m0, s11, 0x11f80
	ds_read_b128 v[146:149], v165
	global_load_lds_dwordx4 v[220:221], off offset:128
	v_mfma_f32_16x16x32_f16 v[82:85], v[86:89], v[134:137], v[82:85]
	ds_read_b128 v[150:153], v165 offset:2048
	v_mfma_f32_16x16x32_f16 v[58:61], v[86:89], v[138:141], v[58:61]
	ds_read_b128 v[154:157], v165 offset:4096
	v_mfma_f32_16x16x32_f16 v[14:17], v[86:89], v[142:145], v[14:17]
	ds_read_b128 v[110:113], v161
	v_mfma_f32_16x16x32_f16 v[78:81], v[90:93], v[134:137], v[78:81]
	ds_read_b128 v[114:117], v161 offset:2048
	v_mfma_f32_16x16x32_f16 v[22:25], v[90:93], v[138:141], v[22:25]
	ds_read_b128 v[118:121], v161 offset:4096
	v_mfma_f32_16x16x32_f16 v[30:33], v[90:93], v[142:145], v[30:33]
	s_add_u32 m0, s11, 0x13f80
	ds_read_b128 v[122:125], v161 offset:6144
	global_load_lds_dwordx4 v[224:225], off offset:128
	v_mfma_f32_16x16x32_f16 v[74:77], v[94:97], v[134:137], v[74:77]
	ds_read_b128 v[126:129], v161 offset:8192
	v_mfma_f32_16x16x32_f16 v[18:21], v[94:97], v[138:141], v[18:21]
	ds_read_b128 v[130:133], v161 offset:10240
	v_mfma_f32_16x16x32_f16 v[26:29], v[94:97], v[142:145], v[26:29]
	v_mfma_f32_16x16x32_f16 v[70:73], v[98:101], v[134:137], v[70:73]
	v_mfma_f32_16x16x32_f16 v[46:49], v[98:101], v[138:141], v[46:49]
	v_mfma_f32_16x16x32_f16 v[240:243], v[98:101], v[142:145], v[240:243]
	s_add_u32 m0, s11, 0x15f80
	s_nop 0
	global_load_lds_dwordx4 v[228:229], off offset:128
	v_mfma_f32_16x16x32_f16 v[66:69], v[102:105], v[134:137], v[66:69]
	v_mfma_f32_16x16x32_f16 v[42:45], v[102:105], v[138:141], v[42:45]
	v_mfma_f32_16x16x32_f16 v[236:239], v[102:105], v[142:145], v[236:239]
	v_mfma_f32_16x16x32_f16 v[62:65], v[106:109], v[134:137], v[62:65]
	v_mfma_f32_16x16x32_f16 v[38:41], v[106:109], v[138:141], v[38:41]
	v_mfma_f32_16x16x32_f16 v[34:37], v[106:109], v[142:145], v[34:37]
	s_waitcnt vmcnt(6) lgkmcnt(0)
	s_barrier
	s_add_u32 m0, s11, 0x17f00
	ds_read_b128 v[134:137], v162
	global_load_lds_dwordx4 v[218:219], off offset:256
	v_mfma_f32_16x16x32_f16 v[82:85], v[110:113], v[146:149], v[82:85]
	ds_read_b128 v[138:141], v162 offset:2048
	v_mfma_f32_16x16x32_f16 v[58:61], v[110:113], v[150:153], v[58:61]
	ds_read_b128 v[142:145], v162 offset:4096
	v_mfma_f32_16x16x32_f16 v[14:17], v[110:113], v[154:157], v[14:17]
	ds_read_b128 v[86:89], v158
	v_mfma_f32_16x16x32_f16 v[78:81], v[114:117], v[146:149], v[78:81]
	ds_read_b128 v[90:93], v158 offset:2048
	v_mfma_f32_16x16x32_f16 v[22:25], v[114:117], v[150:153], v[22:25]
	ds_read_b128 v[94:97], v158 offset:4096
	v_mfma_f32_16x16x32_f16 v[30:33], v[114:117], v[154:157], v[30:33]
	s_add_u32 m0, s11, 0x19f00
	ds_read_b128 v[98:101], v158 offset:6144
	global_load_lds_dwordx4 v[222:223], off offset:256
	v_mfma_f32_16x16x32_f16 v[74:77], v[118:121], v[146:149], v[74:77]
	ds_read_b128 v[102:105], v158 offset:8192
	v_mfma_f32_16x16x32_f16 v[18:21], v[118:121], v[150:153], v[18:21]
	ds_read_b128 v[106:109], v158 offset:10240
	v_mfma_f32_16x16x32_f16 v[26:29], v[118:121], v[154:157], v[26:29]
	v_mfma_f32_16x16x32_f16 v[70:73], v[122:125], v[146:149], v[70:73]
	v_lshl_add_u64 v[220:221], v[220:221], 0, s[20:21]
	v_mfma_f32_16x16x32_f16 v[46:49], v[122:125], v[150:153], v[46:49]
	v_lshl_add_u64 v[224:225], v[224:225], 0, s[20:21]
	v_mfma_f32_16x16x32_f16 v[240:243], v[122:125], v[154:157], v[240:243]
	s_add_u32 m0, s11, 0x1bf00
	s_nop 0
	global_load_lds_dwordx4 v[226:227], off offset:256
	v_mfma_f32_16x16x32_f16 v[66:69], v[126:129], v[146:149], v[66:69]
	v_lshl_add_u64 v[228:229], v[228:229], 0, s[20:21]
	v_mfma_f32_16x16x32_f16 v[42:45], v[126:129], v[150:153], v[42:45]
	v_lshl_add_u64 v[218:219], v[218:219], 0, s[20:21]
	v_mfma_f32_16x16x32_f16 v[236:239], v[126:129], v[154:157], v[236:239]
	v_lshl_add_u64 v[222:223], v[222:223], 0, s[20:21]
	v_mfma_f32_16x16x32_f16 v[62:65], v[130:133], v[146:149], v[62:65]
	v_lshl_add_u64 v[226:227], v[226:227], 0, s[20:21]
	v_mfma_f32_16x16x32_f16 v[38:41], v[130:133], v[150:153], v[38:41]
	v_mfma_f32_16x16x32_f16 v[34:37], v[130:133], v[154:157], v[34:37]
	s_sub_u32 s22, s22, 1
	s_cmp_lg_u32 s22, 0
	s_cbranch_scc1 .Lgemm_N_loop
	s_waitcnt lgkmcnt(0)
	s_add_u32 m0, s11, 0x1e080
	ds_read_b128 v[146:149], v164
	global_load_lds_dwordx4 v[220:221], off offset:-128
	v_mfma_f32_16x16x32_f16 v[82:85], v[86:89], v[134:137], v[82:85]
	ds_read_b128 v[150:153], v164 offset:2048
	v_mfma_f32_16x16x32_f16 v[58:61], v[86:89], v[138:141], v[58:61]
	ds_read_b128 v[154:157], v164 offset:4096
	v_mfma_f32_16x16x32_f16 v[14:17], v[86:89], v[142:145], v[14:17]
	ds_read_b128 v[110:113], v160
	v_mfma_f32_16x16x32_f16 v[78:81], v[90:93], v[134:137], v[78:81]
	ds_read_b128 v[114:117], v160 offset:2048
	v_mfma_f32_16x16x32_f16 v[22:25], v[90:93], v[138:141], v[22:25]
	ds_read_b128 v[118:121], v160 offset:4096
	v_mfma_f32_16x16x32_f16 v[30:33], v[90:93], v[142:145], v[30:33]
	s_add_u32 m0, s11, 0x20080
	ds_read_b128 v[122:125], v160 offset:6144
	global_load_lds_dwordx4 v[224:225], off offset:-128
	v_mfma_f32_16x16x32_f16 v[74:77], v[94:97], v[134:137], v[74:77]
	ds_read_b128 v[126:129], v160 offset:8192
	v_mfma_f32_16x16x32_f16 v[18:21], v[94:97], v[138:141], v[18:21]
	ds_read_b128 v[130:133], v160 offset:10240
	v_mfma_f32_16x16x32_f16 v[26:29], v[94:97], v[142:145], v[26:29]
	v_mfma_f32_16x16x32_f16 v[70:73], v[98:101], v[134:137], v[70:73]
	v_mfma_f32_16x16x32_f16 v[46:49], v[98:101], v[138:141], v[46:49]
	v_mfma_f32_16x16x32_f16 v[240:243], v[98:101], v[142:145], v[240:243]
	s_add_u32 m0, s11, 0x22080
	s_nop 0
	global_load_lds_dwordx4 v[228:229], off offset:-128
	v_mfma_f32_16x16x32_f16 v[66:69], v[102:105], v[134:137], v[66:69]
	v_mfma_f32_16x16x32_f16 v[42:45], v[102:105], v[138:141], v[42:45]
	v_mfma_f32_16x16x32_f16 v[236:239], v[102:105], v[142:145], v[236:239]
	v_mfma_f32_16x16x32_f16 v[62:65], v[106:109], v[134:137], v[62:65]
	v_mfma_f32_16x16x32_f16 v[38:41], v[106:109], v[138:141], v[38:41]
	v_mfma_f32_16x16x32_f16 v[34:37], v[106:109], v[142:145], v[34:37]
	s_waitcnt vmcnt(6) lgkmcnt(0)
	s_barrier
	s_add_u32 m0, s11, 0x0
	ds_read_b128 v[134:137], v162 offset:49152
	global_load_lds_dwordx4 v[218:219], off
	v_mfma_f32_16x16x32_f16 v[82:85], v[110:113], v[146:149], v[82:85]
	ds_read_b128 v[138:141], v162 offset:51200
	v_mfma_f32_16x16x32_f16 v[58:61], v[110:113], v[150:153], v[58:61]
	ds_read_b128 v[142:145], v162 offset:53248
	v_mfma_f32_16x16x32_f16 v[14:17], v[110:113], v[154:157], v[14:17]
	ds_read_b128 v[86:89], v158 offset:49152
	v_mfma_f32_16x16x32_f16 v[78:81], v[114:117], v[146:149], v[78:81]
	ds_read_b128 v[90:93], v158 offset:51200
	v_mfma_f32_16x16x32_f16 v[22:25], v[114:117], v[150:153], v[22:25]
	ds_read_b128 v[94:97], v158 offset:53248
	v_mfma_f32_16x16x32_f16 v[30:33], v[114:117], v[154:157], v[30:33]
	s_add_u32 m0, s11, 0x2000
	ds_read_b128 v[98:101], v158 offset:55296
	global_load_lds_dwordx4 v[222:223], off
	v_mfma_f32_16x16x32_f16 v[74:77], v[118:121], v[146:149], v[74:77]
	ds_read_b128 v[102:105], v158 offset:57344
	v_mfma_f32_16x16x32_f16 v[18:21], v[118:121], v[150:153], v[18:21]
	ds_read_b128 v[106:109], v158 offset:59392
	v_mfma_f32_16x16x32_f16 v[26:29], v[118:121], v[154:157], v[26:29]
	v_mfma_f32_16x16x32_f16 v[70:73], v[122:125], v[146:149], v[70:73]
	v_mfma_f32_16x16x32_f16 v[46:49], v[122:125], v[150:153], v[46:49]
	v_mfma_f32_16x16x32_f16 v[240:243], v[122:125], v[154:157], v[240:243]
	s_add_u32 m0, s11, 0x4000
	s_nop 0
	global_load_lds_dwordx4 v[226:227], off
	v_mfma_f32_16x16x32_f16 v[66:69], v[126:129], v[146:149], v[66:69]
	v_mfma_f32_16x16x32_f16 v[42:45], v[126:129], v[150:153], v[42:45]
	v_mfma_f32_16x16x32_f16 v[236:239], v[126:129], v[154:157], v[236:239]
	v_mfma_f32_16x16x32_f16 v[62:65], v[130:133], v[146:149], v[62:65]
	v_mfma_f32_16x16x32_f16 v[38:41], v[130:133], v[150:153], v[38:41]
	v_mfma_f32_16x16x32_f16 v[34:37], v[130:133], v[154:157], v[34:37]
	s_waitcnt lgkmcnt(0)
	s_add_u32 m0, s11, 0x6000
	ds_read_b128 v[146:149], v164 offset:49152
	global_load_lds_dwordx4 v[220:221], off
	v_mfma_f32_16x16x32_f16 v[82:85], v[86:89], v[134:137], v[82:85]
	ds_read_b128 v[150:153], v164 offset:51200
	v_mfma_f32_16x16x32_f16 v[58:61], v[86:89], v[138:141], v[58:61]
	ds_read_b128 v[154:157], v164 offset:53248
	v_mfma_f32_16x16x32_f16 v[14:17], v[86:89], v[142:145], v[14:17]
	ds_read_b128 v[110:113], v160 offset:49152
	v_mfma_f32_16x16x32_f16 v[78:81], v[90:93], v[134:137], v[78:81]
	ds_read_b128 v[114:117], v160 offset:51200
	v_mfma_f32_16x16x32_f16 v[22:25], v[90:93], v[138:141], v[22:25]
	ds_read_b128 v[118:121], v160 offset:53248
	v_mfma_f32_16x16x32_f16 v[30:33], v[90:93], v[142:145], v[30:33]
	s_add_u32 m0, s11, 0x8000
	ds_read_b128 v[122:125], v160 offset:55296
	global_load_lds_dwordx4 v[224:225], off
	v_mfma_f32_16x16x32_f16 v[74:77], v[94:97], v[134:137], v[74:77]
	ds_read_b128 v[126:129], v160 offset:57344
	v_mfma_f32_16x16x32_f16 v[18:21], v[94:97], v[138:141], v[18:21]
	ds_read_b128 v[130:133], v160 offset:59392
	v_mfma_f32_16x16x32_f16 v[26:29], v[94:97], v[142:145], v[26:29]
	v_mfma_f32_16x16x32_f16 v[70:73], v[98:101], v[134:137], v[70:73]
	v_mfma_f32_16x16x32_f16 v[46:49], v[98:101], v[138:141], v[46:49]
	v_mfma_f32_16x16x32_f16 v[240:243], v[98:101], v[142:145], v[240:243]
	s_add_u32 m0, s11, 0xa000
	s_nop 0
	global_load_lds_dwordx4 v[228:229], off
	v_mfma_f32_16x16x32_f16 v[66:69], v[102:105], v[134:137], v[66:69]
	v_mfma_f32_16x16x32_f16 v[42:45], v[102:105], v[138:141], v[42:45]
	v_mfma_f32_16x16x32_f16 v[236:239], v[102:105], v[142:145], v[236:239]
	v_mfma_f32_16x16x32_f16 v[62:65], v[106:109], v[134:137], v[62:65]
	v_mfma_f32_16x16x32_f16 v[38:41], v[106:109], v[138:141], v[38:41]
	v_mfma_f32_16x16x32_f16 v[34:37], v[106:109], v[142:145], v[34:37]
	s_waitcnt vmcnt(6) lgkmcnt(0)
	s_barrier
	s_lshl_b32 s26, s17, 2
	s_add_u32 s26, s24, s26
	s_addc_u32 s27, s25, 0
	v_lshlrev_b32_e32 v50, 2, v1
	global_load_dword v234, v50, s[26:27]
	global_load_dword v232, v50, s[26:27] offset:64
	global_load_dword v230, v50, s[26:27] offset:128
	ds_read_b128 v[134:137], v163
	v_mfma_f32_16x16x32_f16 v[82:85], v[110:113], v[146:149], v[82:85]
	ds_read_b128 v[138:141], v163 offset:2048
	v_mfma_f32_16x16x32_f16 v[58:61], v[110:113], v[150:153], v[58:61]
	ds_read_b128 v[142:145], v163 offset:4096
	v_mfma_f32_16x16x32_f16 v[14:17], v[110:113], v[154:157], v[14:17]
	ds_read_b128 v[86:89], v159
	v_mfma_f32_16x16x32_f16 v[78:81], v[114:117], v[146:149], v[78:81]
	ds_read_b128 v[90:93], v159 offset:2048
	v_mfma_f32_16x16x32_f16 v[22:25], v[114:117], v[150:153], v[22:25]
	ds_read_b128 v[94:97], v159 offset:4096
	v_mfma_f32_16x16x32_f16 v[30:33], v[114:117], v[154:157], v[30:33]
	ds_read_b128 v[98:101], v159 offset:6144
	v_mfma_f32_16x16x32_f16 v[74:77], v[118:121], v[146:149], v[74:77]
	ds_read_b128 v[102:105], v159 offset:8192
	v_mfma_f32_16x16x32_f16 v[18:21], v[118:121], v[150:153], v[18:21]
	ds_read_b128 v[106:109], v159 offset:10240
	v_mfma_f32_16x16x32_f16 v[26:29], v[118:121], v[154:157], v[26:29]
	v_mfma_f32_16x16x32_f16 v[70:73], v[122:125], v[146:149], v[70:73]
	v_mfma_f32_16x16x32_f16 v[46:49], v[122:125], v[150:153], v[46:49]
	v_mfma_f32_16x16x32_f16 v[240:243], v[122:125], v[154:157], v[240:243]
	v_mfma_f32_16x16x32_f16 v[66:69], v[126:129], v[146:149], v[66:69]
	v_mfma_f32_16x16x32_f16 v[42:45], v[126:129], v[150:153], v[42:45]
	v_mfma_f32_16x16x32_f16 v[236:239], v[126:129], v[154:157], v[236:239]
	v_mfma_f32_16x16x32_f16 v[62:65], v[130:133], v[146:149], v[62:65]
	v_mfma_f32_16x16x32_f16 v[38:41], v[130:133], v[150:153], v[38:41]
	v_mfma_f32_16x16x32_f16 v[34:37], v[130:133], v[154:157], v[34:37]
	s_waitcnt lgkmcnt(0)
	ds_read_b128 v[146:149], v165
	v_mfma_f32_16x16x32_f16 v[82:85], v[86:89], v[134:137], v[82:85]
	ds_read_b128 v[150:153], v165 offset:2048
	v_mfma_f32_16x16x32_f16 v[58:61], v[86:89], v[138:141], v[58:61]
	ds_read_b128 v[154:157], v165 offset:4096
	v_mfma_f32_16x16x32_f16 v[14:17], v[86:89], v[142:145], v[14:17]
	ds_read_b128 v[110:113], v161
	v_mfma_f32_16x16x32_f16 v[78:81], v[90:93], v[134:137], v[78:81]
	ds_read_b128 v[114:117], v161 offset:2048
	v_mfma_f32_16x16x32_f16 v[22:25], v[90:93], v[138:141], v[22:25]
	ds_read_b128 v[118:121], v161 offset:4096
	v_mfma_f32_16x16x32_f16 v[30:33], v[90:93], v[142:145], v[30:33]
	ds_read_b128 v[122:125], v161 offset:6144
	v_mfma_f32_16x16x32_f16 v[74:77], v[94:97], v[134:137], v[74:77]
	ds_read_b128 v[126:129], v161 offset:8192
	v_mfma_f32_16x16x32_f16 v[18:21], v[94:97], v[138:141], v[18:21]
	ds_read_b128 v[130:133], v161 offset:10240
	v_mfma_f32_16x16x32_f16 v[26:29], v[94:97], v[142:145], v[26:29]
	v_mfma_f32_16x16x32_f16 v[70:73], v[98:101], v[134:137], v[70:73]
	v_mfma_f32_16x16x32_f16 v[46:49], v[98:101], v[138:141], v[46:49]
	v_mfma_f32_16x16x32_f16 v[240:243], v[98:101], v[142:145], v[240:243]
	v_mfma_f32_16x16x32_f16 v[66:69], v[102:105], v[134:137], v[66:69]
	v_mfma_f32_16x16x32_f16 v[42:45], v[102:105], v[138:141], v[42:45]
	v_mfma_f32_16x16x32_f16 v[236:239], v[102:105], v[142:145], v[236:239]
	v_mfma_f32_16x16x32_f16 v[62:65], v[106:109], v[134:137], v[62:65]
	v_mfma_f32_16x16x32_f16 v[38:41], v[106:109], v[138:141], v[38:41]
	v_mfma_f32_16x16x32_f16 v[34:37], v[106:109], v[142:145], v[34:37]
	s_waitcnt vmcnt(3) lgkmcnt(0)
	s_barrier
	ds_read_b128 v[134:137], v162
	v_mfma_f32_16x16x32_f16 v[82:85], v[110:113], v[146:149], v[82:85]
	ds_read_b128 v[138:141], v162 offset:2048
	v_mfma_f32_16x16x32_f16 v[58:61], v[110:113], v[150:153], v[58:61]
	ds_read_b128 v[142:145], v162 offset:4096
	v_mfma_f32_16x16x32_f16 v[14:17], v[110:113], v[154:157], v[14:17]
	ds_read_b128 v[86:89], v158
	v_mfma_f32_16x16x32_f16 v[78:81], v[114:117], v[146:149], v[78:81]
	ds_read_b128 v[90:93], v158 offset:2048
	v_mfma_f32_16x16x32_f16 v[22:25], v[114:117], v[150:153], v[22:25]
	ds_read_b128 v[94:97], v158 offset:4096
	v_mfma_f32_16x16x32_f16 v[30:33], v[114:117], v[154:157], v[30:33]
	ds_read_b128 v[98:101], v158 offset:6144
	v_mfma_f32_16x16x32_f16 v[74:77], v[118:121], v[146:149], v[74:77]
	ds_read_b128 v[102:105], v158 offset:8192
	v_mfma_f32_16x16x32_f16 v[18:21], v[118:121], v[150:153], v[18:21]
	ds_read_b128 v[106:109], v158 offset:10240
	v_mfma_f32_16x16x32_f16 v[26:29], v[118:121], v[154:157], v[26:29]
	v_mfma_f32_16x16x32_f16 v[70:73], v[122:125], v[146:149], v[70:73]
	v_mfma_f32_16x16x32_f16 v[46:49], v[122:125], v[150:153], v[46:49]
	v_mfma_f32_16x16x32_f16 v[240:243], v[122:125], v[154:157], v[240:243]
	v_mfma_f32_16x16x32_f16 v[66:69], v[126:129], v[146:149], v[66:69]
	v_mfma_f32_16x16x32_f16 v[42:45], v[126:129], v[150:153], v[42:45]
	v_mfma_f32_16x16x32_f16 v[236:239], v[126:129], v[154:157], v[236:239]
	v_mfma_f32_16x16x32_f16 v[62:65], v[130:133], v[146:149], v[62:65]
	v_mfma_f32_16x16x32_f16 v[38:41], v[130:133], v[150:153], v[38:41]
	v_mfma_f32_16x16x32_f16 v[34:37], v[130:133], v[154:157], v[34:37]
	s_waitcnt lgkmcnt(0)
	ds_read_b128 v[146:149], v164
	v_mfma_f32_16x16x32_f16 v[82:85], v[86:89], v[134:137], v[82:85]
	ds_read_b128 v[150:153], v164 offset:2048
	v_mfma_f32_16x16x32_f16 v[58:61], v[86:89], v[138:141], v[58:61]
	ds_read_b128 v[154:157], v164 offset:4096
	v_mfma_f32_16x16x32_f16 v[14:17], v[86:89], v[142:145], v[14:17]
	ds_read_b128 v[110:113], v160
	v_mfma_f32_16x16x32_f16 v[78:81], v[90:93], v[134:137], v[78:81]
	ds_read_b128 v[114:117], v160 offset:2048
	v_mfma_f32_16x16x32_f16 v[22:25], v[90:93], v[138:141], v[22:25]
	ds_read_b128 v[118:121], v160 offset:4096
	v_mfma_f32_16x16x32_f16 v[30:33], v[90:93], v[142:145], v[30:33]
	ds_read_b128 v[122:125], v160 offset:6144
	v_mfma_f32_16x16x32_f16 v[74:77], v[94:97], v[134:137], v[74:77]
	ds_read_b128 v[126:129], v160 offset:8192
	v_mfma_f32_16x16x32_f16 v[18:21], v[94:97], v[138:141], v[18:21]
	ds_read_b128 v[130:133], v160 offset:10240
	v_mfma_f32_16x16x32_f16 v[26:29], v[94:97], v[142:145], v[26:29]
	v_mfma_f32_16x16x32_f16 v[70:73], v[98:101], v[134:137], v[70:73]
	v_mfma_f32_16x16x32_f16 v[46:49], v[98:101], v[138:141], v[46:49]
	v_mfma_f32_16x16x32_f16 v[240:243], v[98:101], v[142:145], v[240:243]
	v_mfma_f32_16x16x32_f16 v[66:69], v[102:105], v[134:137], v[66:69]
	v_mfma_f32_16x16x32_f16 v[42:45], v[102:105], v[138:141], v[42:45]
	v_mfma_f32_16x16x32_f16 v[236:239], v[102:105], v[142:145], v[236:239]
	v_mfma_f32_16x16x32_f16 v[62:65], v[106:109], v[134:137], v[62:65]
	v_mfma_f32_16x16x32_f16 v[38:41], v[106:109], v[138:141], v[38:41]
	v_mfma_f32_16x16x32_f16 v[34:37], v[106:109], v[142:145], v[34:37]
	s_waitcnt lgkmcnt(0)
	v_mfma_f32_16x16x32_f16 v[82:85], v[110:113], v[146:149], v[82:85]
	v_mfma_f32_16x16x32_f16 v[58:61], v[110:113], v[150:153], v[58:61]
	v_mfma_f32_16x16x32_f16 v[14:17], v[110:113], v[154:157], v[14:17]
	v_mfma_f32_16x16x32_f16 v[78:81], v[114:117], v[146:149], v[78:81]
	v_mfma_f32_16x16x32_f16 v[22:25], v[114:117], v[150:153], v[22:25]
	v_mfma_f32_16x16x32_f16 v[30:33], v[114:117], v[154:157], v[30:33]
	v_mfma_f32_16x16x32_f16 v[74:77], v[118:121], v[146:149], v[74:77]
	v_mfma_f32_16x16x32_f16 v[18:21], v[118:121], v[150:153], v[18:21]
	v_mfma_f32_16x16x32_f16 v[26:29], v[118:121], v[154:157], v[26:29]
	v_mfma_f32_16x16x32_f16 v[70:73], v[122:125], v[146:149], v[70:73]
	v_mfma_f32_16x16x32_f16 v[46:49], v[122:125], v[150:153], v[46:49]
	v_mfma_f32_16x16x32_f16 v[240:243], v[122:125], v[154:157], v[240:243]
	v_mfma_f32_16x16x32_f16 v[66:69], v[126:129], v[146:149], v[66:69]
	v_mfma_f32_16x16x32_f16 v[42:45], v[126:129], v[150:153], v[42:45]
	v_mfma_f32_16x16x32_f16 v[236:239], v[126:129], v[154:157], v[236:239]
	v_mfma_f32_16x16x32_f16 v[62:65], v[130:133], v[146:149], v[62:65]
	v_mfma_f32_16x16x32_f16 v[38:41], v[130:133], v[150:153], v[38:41]
	v_mfma_f32_16x16x32_f16 v[34:37], v[130:133], v[154:157], v[34:37]
